# adds: hyena conv context-unit epilogue requests its w/x0 pieces in 3 batches instead of 32 dependent round trips
# baseline (speedup 1.0000x reference)
.LBB0_817:
	s_add_i32 s17, s14, 0xfffffef0
	s_add_i32 s20, s14, 0xffffff10
	s_cmp_lt_u32 s20, s16
	s_cselect_b32 s18, s20, s17
	s_ashr_i32 s19, s18, 31
	s_waitcnt vmcnt(1)
	v_mfma_f32_32x32x16_bf16 v[18:33], v[184:187], v[196:199], v[18:33]
	v_lshl_add_u64 v[184:185], s[18:19], 1, v[232:233]
	global_load_dwordx4 v[208:211], v[184:185], off
	v_add_lshl_u32 v249, v248, s14, 1
	v_add_u32_e32 v184, 0xfffffde0, v249
	v_and_b32_e32 v184, -4, v184
	v_add_u32_e32 v200, s0, v184
	ds_read2_b32 v[184:185], v200 offset1:1
	ds_read2_b32 v[186:187], v200 offset0:1 offset1:2
	ds_read2_b32 v[200:201], v200 offset0:3 offset1:4
	v_mfma_f32_32x32x16_bf16 v[36:51], v[176:179], v[196:199], v[36:51]
	v_mfma_f32_32x32x16_bf16 v[52:67], v[168:171], v[196:199], v[52:67]
	v_mfma_f32_32x32x16_bf16 v[68:83], v[156:159], v[196:199], v[68:83]
	v_mfma_f32_32x32x16_bf16 v[84:99], v[148:151], v[196:199], v[84:99]
	v_mfma_f32_32x32x16_bf16 v[100:115], v[140:143], v[196:199], v[100:115]
	v_mfma_f32_32x32x16_bf16 v[2:17], v[132:135], v[196:199], v[2:17]
	s_waitcnt lgkmcnt(0)
	v_alignbit_b32 v203, v201, v200, v35
	v_alignbit_b32 v202, v200, v187, v166
	v_alignbit_b32 v201, v187, v185, v1
	v_alignbit_b32 v200, v186, v184, v164
	s_add_i32 s17, s14, 0xffffff00
	s_add_i32 s29, s14, 0xffffff20
	s_cmp_lt_u32 s29, s16
	s_cselect_b32 s18, s29, s17
	s_ashr_i32 s19, s18, 31
	v_lshl_add_u64 v[184:185], s[18:19], 1, v[232:233]
	v_mfma_f32_32x32x16_bf16 v[116:131], v[200:203], v[196:199], v[116:131]
	global_load_dwordx4 v[196:199], v[184:185], off
	v_add_u32_e32 v184, 0xfffffe00, v249
	v_and_b32_e32 v184, -4, v184
	s_waitcnt vmcnt(2)
	v_mfma_f32_32x32x16_bf16 v[18:33], v[188:191], v[192:195], v[18:33]
	v_add_u32_e32 v188, s0, v184
	ds_read2_b32 v[184:185], v188 offset1:1
	ds_read2_b32 v[186:187], v188 offset0:1 offset1:2
	ds_read2_b32 v[188:189], v188 offset0:3 offset1:4
	v_mfma_f32_32x32x16_bf16 v[36:51], v[180:183], v[192:195], v[36:51]
	v_mfma_f32_32x32x16_bf16 v[52:67], v[172:175], v[192:195], v[52:67]
	v_mfma_f32_32x32x16_bf16 v[68:83], v[160:163], v[192:195], v[68:83]
	v_mfma_f32_32x32x16_bf16 v[84:99], v[152:155], v[192:195], v[84:99]
	v_mfma_f32_32x32x16_bf16 v[100:115], v[144:147], v[192:195], v[100:115]
	v_mfma_f32_32x32x16_bf16 v[2:17], v[136:139], v[192:195], v[2:17]
	s_waitcnt lgkmcnt(0)
	v_alignbit_b32 v207, v189, v188, v35
	v_alignbit_b32 v206, v188, v187, v166
	v_alignbit_b32 v205, v187, v185, v1
	v_alignbit_b32 v204, v186, v184, v164
	s_add_i32 s17, s14, 0xffffff30
	s_cmp_lt_u32 s17, s16
	s_cselect_b32 s18, s17, s20
	s_ashr_i32 s19, s18, 31
	s_waitcnt vmcnt(1)
	v_mfma_f32_32x32x16_bf16 v[18:33], v[176:179], v[208:211], v[18:33]
	v_lshl_add_u64 v[176:177], s[18:19], 1, v[232:233]
	v_mfma_f32_32x32x16_bf16 v[116:131], v[204:207], v[192:195], v[116:131]
	global_load_dwordx4 v[192:195], v[176:177], off
	v_add_u32_e32 v176, 0xfffffe20, v249
	v_and_b32_e32 v176, -4, v176
	v_add_u32_e32 v184, s0, v176
	ds_read2_b32 v[176:177], v184 offset1:1
	ds_read2_b32 v[178:179], v184 offset0:1 offset1:2
	ds_read2_b32 v[184:185], v184 offset0:3 offset1:4
	v_mfma_f32_32x32x16_bf16 v[36:51], v[168:171], v[208:211], v[36:51]
	v_mfma_f32_32x32x16_bf16 v[52:67], v[156:159], v[208:211], v[52:67]
	v_mfma_f32_32x32x16_bf16 v[68:83], v[148:151], v[208:211], v[68:83]
	v_mfma_f32_32x32x16_bf16 v[84:99], v[140:143], v[208:211], v[84:99]
	v_mfma_f32_32x32x16_bf16 v[100:115], v[132:135], v[208:211], v[100:115]
	v_mfma_f32_32x32x16_bf16 v[2:17], v[200:203], v[208:211], v[2:17]
	s_waitcnt lgkmcnt(0)
	v_alignbit_b32 v187, v185, v184, v35
	v_alignbit_b32 v186, v184, v179, v166
	v_alignbit_b32 v185, v179, v177, v1
	v_alignbit_b32 v184, v178, v176, v164
	s_add_i32 s20, s14, 0xffffff40
	s_cmp_lt_u32 s20, s16
	s_cselect_b32 s18, s20, s29
	s_ashr_i32 s19, s18, 31
	v_lshl_add_u64 v[176:177], s[18:19], 1, v[232:233]
	v_mfma_f32_32x32x16_bf16 v[116:131], v[184:187], v[208:211], v[116:131]
	global_load_dwordx4 v[208:211], v[176:177], off
	v_add_u32_e32 v176, 0xfffffe40, v249
	v_and_b32_e32 v176, -4, v176
	s_waitcnt vmcnt(2)
	v_mfma_f32_32x32x16_bf16 v[18:33], v[180:183], v[196:199], v[18:33]
	v_add_u32_e32 v180, s0, v176
	ds_read2_b32 v[176:177], v180 offset1:1
	ds_read2_b32 v[178:179], v180 offset0:1 offset1:2
	ds_read2_b32 v[180:181], v180 offset0:3 offset1:4
	v_mfma_f32_32x32x16_bf16 v[36:51], v[172:175], v[196:199], v[36:51]
	v_mfma_f32_32x32x16_bf16 v[52:67], v[160:163], v[196:199], v[52:67]
	v_mfma_f32_32x32x16_bf16 v[68:83], v[152:155], v[196:199], v[68:83]
	v_mfma_f32_32x32x16_bf16 v[84:99], v[144:147], v[196:199], v[84:99]
	v_mfma_f32_32x32x16_bf16 v[100:115], v[136:139], v[196:199], v[100:115]
	v_mfma_f32_32x32x16_bf16 v[2:17], v[204:207], v[196:199], v[2:17]
	s_waitcnt lgkmcnt(0)
	v_alignbit_b32 v191, v181, v180, v35
	v_alignbit_b32 v190, v180, v179, v166
	v_alignbit_b32 v189, v179, v177, v1
	v_alignbit_b32 v188, v178, v176, v164
	s_add_i32 s29, s14, 0xffffff50
	s_cmp_lt_u32 s29, s16
	s_cselect_b32 s18, s29, s17
	s_ashr_i32 s19, s18, 31
	s_waitcnt vmcnt(1)
	v_mfma_f32_32x32x16_bf16 v[18:33], v[168:171], v[192:195], v[18:33]
	v_lshl_add_u64 v[168:169], s[18:19], 1, v[232:233]
	v_mfma_f32_32x32x16_bf16 v[116:131], v[188:191], v[196:199], v[116:131]
	global_load_dwordx4 v[196:199], v[168:169], off
	v_add_u32_e32 v168, 0xfffffe60, v249
	v_and_b32_e32 v168, -4, v168
	v_add_u32_e32 v176, s0, v168
	ds_read2_b32 v[168:169], v176 offset1:1
	ds_read2_b32 v[170:171], v176 offset0:1 offset1:2
	ds_read2_b32 v[176:177], v176 offset0:3 offset1:4
	v_mfma_f32_32x32x16_bf16 v[36:51], v[156:159], v[192:195], v[36:51]
	v_mfma_f32_32x32x16_bf16 v[52:67], v[148:151], v[192:195], v[52:67]
	v_mfma_f32_32x32x16_bf16 v[68:83], v[140:143], v[192:195], v[68:83]
	v_mfma_f32_32x32x16_bf16 v[84:99], v[132:135], v[192:195], v[84:99]
	v_mfma_f32_32x32x16_bf16 v[100:115], v[200:203], v[192:195], v[100:115]
	v_mfma_f32_32x32x16_bf16 v[2:17], v[184:187], v[192:195], v[2:17]
	s_waitcnt lgkmcnt(0)
	v_alignbit_b32 v179, v177, v176, v35
	v_alignbit_b32 v178, v176, v171, v166
	v_alignbit_b32 v177, v171, v169, v1
	v_alignbit_b32 v176, v170, v168, v164
	s_add_i32 s17, s14, 0xffffff60
	s_cmp_lt_u32 s17, s16
	s_cselect_b32 s18, s17, s20
	s_ashr_i32 s19, s18, 31
	v_lshl_add_u64 v[168:169], s[18:19], 1, v[232:233]
	v_mfma_f32_32x32x16_bf16 v[116:131], v[176:179], v[192:195], v[116:131]
	global_load_dwordx4 v[192:195], v[168:169], off
	v_add_u32_e32 v168, 0xfffffe80, v249
	v_and_b32_e32 v168, -4, v168
	s_waitcnt vmcnt(2)
	v_mfma_f32_32x32x16_bf16 v[18:33], v[172:175], v[208:211], v[18:33]
	v_add_u32_e32 v172, s0, v168
	ds_read2_b32 v[168:169], v172 offset1:1
	ds_read2_b32 v[170:171], v172 offset0:1 offset1:2
	ds_read2_b32 v[172:173], v172 offset0:3 offset1:4
	v_mfma_f32_32x32x16_bf16 v[36:51], v[160:163], v[208:211], v[36:51]
	v_mfma_f32_32x32x16_bf16 v[52:67], v[152:155], v[208:211], v[52:67]
	v_mfma_f32_32x32x16_bf16 v[68:83], v[144:147], v[208:211], v[68:83]
	v_mfma_f32_32x32x16_bf16 v[84:99], v[136:139], v[208:211], v[84:99]
	v_mfma_f32_32x32x16_bf16 v[100:115], v[204:207], v[208:211], v[100:115]
	v_mfma_f32_32x32x16_bf16 v[2:17], v[188:191], v[208:211], v[2:17]
	s_waitcnt lgkmcnt(0)
	v_alignbit_b32 v183, v173, v172, v35
	v_alignbit_b32 v182, v172, v171, v166
	v_alignbit_b32 v181, v171, v169, v1
	v_alignbit_b32 v180, v170, v168, v164
	s_add_i32 s20, s14, 0xffffff70
	s_cmp_lt_u32 s20, s16
	s_cselect_b32 s18, s20, s29
	s_ashr_i32 s19, s18, 31
	s_waitcnt vmcnt(1)
	v_mfma_f32_32x32x16_bf16 v[18:33], v[156:159], v[196:199], v[18:33]
	v_lshl_add_u64 v[156:157], s[18:19], 1, v[232:233]
	v_mfma_f32_32x32x16_bf16 v[116:131], v[180:183], v[208:211], v[116:131]
	global_load_dwordx4 v[208:211], v[156:157], off
	v_add_u32_e32 v156, 0xfffffea0, v249
	v_and_b32_e32 v156, -4, v156
	v_add_u32_e32 v168, s0, v156
	ds_read2_b32 v[156:157], v168 offset1:1
	ds_read2_b32 v[158:159], v168 offset0:1 offset1:2
	ds_read2_b32 v[168:169], v168 offset0:3 offset1:4
	v_mfma_f32_32x32x16_bf16 v[36:51], v[148:151], v[196:199], v[36:51]
	v_mfma_f32_32x32x16_bf16 v[52:67], v[140:143], v[196:199], v[52:67]
	v_mfma_f32_32x32x16_bf16 v[68:83], v[132:135], v[196:199], v[68:83]
	v_mfma_f32_32x32x16_bf16 v[84:99], v[200:203], v[196:199], v[84:99]
	v_mfma_f32_32x32x16_bf16 v[100:115], v[184:187], v[196:199], v[100:115]
	v_mfma_f32_32x32x16_bf16 v[2:17], v[176:179], v[196:199], v[2:17]
	s_waitcnt lgkmcnt(0)
	v_alignbit_b32 v171, v169, v168, v35
	v_alignbit_b32 v170, v168, v159, v166
	v_alignbit_b32 v169, v159, v157, v1
	v_alignbit_b32 v168, v158, v156, v164
	s_add_i32 s29, s14, 0xffffff80
	s_cmp_lt_u32 s29, s16
	s_cselect_b32 s18, s29, s17
	s_ashr_i32 s19, s18, 31
	v_lshl_add_u64 v[156:157], s[18:19], 1, v[232:233]
	v_mfma_f32_32x32x16_bf16 v[116:131], v[168:171], v[196:199], v[116:131]
	global_load_dwordx4 v[196:199], v[156:157], off
	v_add_u32_e32 v156, 0xfffffec0, v249
	v_and_b32_e32 v156, -4, v156
	s_waitcnt vmcnt(2)
	v_mfma_f32_32x32x16_bf16 v[18:33], v[160:163], v[192:195], v[18:33]
	v_add_u32_e32 v160, s0, v156
	ds_read2_b32 v[156:157], v160 offset1:1
	ds_read2_b32 v[158:159], v160 offset0:1 offset1:2
	ds_read2_b32 v[160:161], v160 offset0:3 offset1:4
	v_mfma_f32_32x32x16_bf16 v[36:51], v[152:155], v[192:195], v[36:51]
	v_mfma_f32_32x32x16_bf16 v[52:67], v[144:147], v[192:195], v[52:67]
	v_mfma_f32_32x32x16_bf16 v[68:83], v[136:139], v[192:195], v[68:83]
	v_mfma_f32_32x32x16_bf16 v[84:99], v[204:207], v[192:195], v[84:99]
	v_mfma_f32_32x32x16_bf16 v[100:115], v[188:191], v[192:195], v[100:115]
	v_mfma_f32_32x32x16_bf16 v[2:17], v[180:183], v[192:195], v[2:17]
	s_waitcnt lgkmcnt(0)
	v_alignbit_b32 v175, v161, v160, v35
	v_alignbit_b32 v174, v160, v159, v166
	v_alignbit_b32 v173, v159, v157, v1
	v_alignbit_b32 v172, v158, v156, v164
	s_add_i32 s17, s14, 0xffffff90
	s_cmp_lt_u32 s17, s16
	s_cselect_b32 s18, s17, s20
	s_ashr_i32 s19, s18, 31
	s_waitcnt vmcnt(1)
	v_mfma_f32_32x32x16_bf16 v[18:33], v[148:151], v[208:211], v[18:33]
	v_lshl_add_u64 v[148:149], s[18:19], 1, v[232:233]
	v_mfma_f32_32x32x16_bf16 v[116:131], v[172:175], v[192:195], v[116:131]
	global_load_dwordx4 v[192:195], v[148:149], off
	v_add_u32_e32 v148, 0xfffffee0, v249
	v_and_b32_e32 v148, -4, v148
	v_add_u32_e32 v156, s0, v148
	ds_read2_b32 v[148:149], v156 offset1:1
	ds_read2_b32 v[150:151], v156 offset0:1 offset1:2
	ds_read2_b32 v[156:157], v156 offset0:3 offset1:4
	v_mfma_f32_32x32x16_bf16 v[36:51], v[140:143], v[208:211], v[36:51]
	v_mfma_f32_32x32x16_bf16 v[52:67], v[132:135], v[208:211], v[52:67]
	v_mfma_f32_32x32x16_bf16 v[68:83], v[200:203], v[208:211], v[68:83]
	v_mfma_f32_32x32x16_bf16 v[84:99], v[184:187], v[208:211], v[84:99]
	v_mfma_f32_32x32x16_bf16 v[100:115], v[176:179], v[208:211], v[100:115]
	v_mfma_f32_32x32x16_bf16 v[2:17], v[168:171], v[208:211], v[2:17]
	s_waitcnt lgkmcnt(0)
	v_alignbit_b32 v159, v157, v156, v35
	v_alignbit_b32 v158, v156, v151, v166
	v_alignbit_b32 v157, v151, v149, v1
	v_alignbit_b32 v156, v150, v148, v164
	s_add_i32 s20, s14, 0xffffffa0
	s_cmp_lt_u32 s20, s16
	s_cselect_b32 s18, s20, s29
	s_ashr_i32 s19, s18, 31
	v_lshl_add_u64 v[148:149], s[18:19], 1, v[232:233]
	v_mfma_f32_32x32x16_bf16 v[116:131], v[156:159], v[208:211], v[116:131]
	global_load_dwordx4 v[208:211], v[148:149], off
	v_add_u32_e32 v148, 0xffffff00, v249
	v_and_b32_e32 v148, -4, v148
	s_waitcnt vmcnt(2)
	v_mfma_f32_32x32x16_bf16 v[18:33], v[152:155], v[196:199], v[18:33]
	v_add_u32_e32 v152, s0, v148
	ds_read2_b32 v[148:149], v152 offset1:1
	ds_read2_b32 v[150:151], v152 offset0:1 offset1:2
	ds_read2_b32 v[152:153], v152 offset0:3 offset1:4
	v_mfma_f32_32x32x16_bf16 v[36:51], v[144:147], v[196:199], v[36:51]
	v_mfma_f32_32x32x16_bf16 v[52:67], v[136:139], v[196:199], v[52:67]
	v_mfma_f32_32x32x16_bf16 v[68:83], v[204:207], v[196:199], v[68:83]
	v_mfma_f32_32x32x16_bf16 v[84:99], v[188:191], v[196:199], v[84:99]
	v_mfma_f32_32x32x16_bf16 v[100:115], v[180:183], v[196:199], v[100:115]
	v_mfma_f32_32x32x16_bf16 v[2:17], v[172:175], v[196:199], v[2:17]
	s_waitcnt lgkmcnt(0)
	v_alignbit_b32 v163, v153, v152, v35
	v_alignbit_b32 v162, v152, v151, v166
	v_alignbit_b32 v161, v151, v149, v1
	v_alignbit_b32 v160, v150, v148, v164
	s_add_i32 s29, s14, 0xffffffb0
	s_cmp_lt_u32 s29, s16
	s_cselect_b32 s18, s29, s17
	s_ashr_i32 s19, s18, 31
	s_waitcnt vmcnt(1)
	v_mfma_f32_32x32x16_bf16 v[18:33], v[140:143], v[192:195], v[18:33]
	v_lshl_add_u64 v[140:141], s[18:19], 1, v[232:233]
	v_mfma_f32_32x32x16_bf16 v[116:131], v[160:163], v[196:199], v[116:131]
	global_load_dwordx4 v[196:199], v[140:141], off
	v_add_u32_e32 v140, 0xffffff20, v249
	v_and_b32_e32 v140, -4, v140
	v_add_u32_e32 v148, s0, v140
	ds_read2_b32 v[140:141], v148 offset1:1
	ds_read2_b32 v[142:143], v148 offset0:1 offset1:2
	ds_read2_b32 v[148:149], v148 offset0:3 offset1:4
	v_mfma_f32_32x32x16_bf16 v[36:51], v[132:135], v[192:195], v[36:51]
	v_mfma_f32_32x32x16_bf16 v[52:67], v[200:203], v[192:195], v[52:67]
	v_mfma_f32_32x32x16_bf16 v[68:83], v[184:187], v[192:195], v[68:83]
	v_mfma_f32_32x32x16_bf16 v[84:99], v[176:179], v[192:195], v[84:99]
	v_mfma_f32_32x32x16_bf16 v[100:115], v[168:171], v[192:195], v[100:115]
	v_mfma_f32_32x32x16_bf16 v[2:17], v[156:159], v[192:195], v[2:17]
	s_waitcnt lgkmcnt(0)
	v_alignbit_b32 v151, v149, v148, v35
	v_alignbit_b32 v150, v148, v143, v166
	v_alignbit_b32 v149, v143, v141, v1
	v_alignbit_b32 v148, v142, v140, v164
	s_sub_i32 s17, s14, 64
	s_cmp_lt_u32 s17, s16
	s_cselect_b32 s18, s17, s20
	s_ashr_i32 s19, s18, 31
	v_lshl_add_u64 v[140:141], s[18:19], 1, v[232:233]
	v_mfma_f32_32x32x16_bf16 v[116:131], v[148:151], v[192:195], v[116:131]
	global_load_dwordx4 v[192:195], v[140:141], off
	v_add_u32_e32 v140, 0xffffff40, v249
	v_and_b32_e32 v140, -4, v140
	s_waitcnt vmcnt(2)
	v_mfma_f32_32x32x16_bf16 v[18:33], v[144:147], v[208:211], v[18:33]
	v_add_u32_e32 v144, s0, v140
	ds_read2_b32 v[140:141], v144 offset1:1
	ds_read2_b32 v[142:143], v144 offset0:1 offset1:2
	ds_read2_b32 v[144:145], v144 offset0:3 offset1:4
	v_mfma_f32_32x32x16_bf16 v[36:51], v[136:139], v[208:211], v[36:51]
	v_mfma_f32_32x32x16_bf16 v[52:67], v[204:207], v[208:211], v[52:67]
	v_mfma_f32_32x32x16_bf16 v[68:83], v[188:191], v[208:211], v[68:83]
	v_mfma_f32_32x32x16_bf16 v[84:99], v[180:183], v[208:211], v[84:99]
	v_mfma_f32_32x32x16_bf16 v[100:115], v[172:175], v[208:211], v[100:115]
	v_mfma_f32_32x32x16_bf16 v[2:17], v[160:163], v[208:211], v[2:17]
	s_sub_i32 s20, s14, 48
	s_cmp_lt_u32 s20, s16
	s_cselect_b32 s18, s20, s29
	s_ashr_i32 s19, s18, 31
	s_waitcnt vmcnt(1)
	v_mfma_f32_32x32x16_bf16 v[18:33], v[132:135], v[196:199], v[18:33]
	v_lshl_add_u64 v[132:133], s[18:19], 1, v[232:233]
	global_load_dwordx4 v[250:253], v[132:133], off
	s_waitcnt lgkmcnt(0)
	v_alignbit_b32 v155, v145, v144, v35
	v_alignbit_b32 v154, v144, v143, v166
	v_alignbit_b32 v153, v143, v141, v1
	v_alignbit_b32 v152, v142, v140, v164
	v_add_u32_e32 v132, 0xffffff60, v249
	v_mfma_f32_32x32x16_bf16 v[36:51], v[200:203], v[196:199], v[36:51]
	v_and_b32_e32 v132, -4, v132
	v_add_u32_e32 v140, s0, v132
	ds_read2_b32 v[132:133], v140 offset1:1
	ds_read2_b32 v[134:135], v140 offset0:1 offset1:2
	ds_read2_b32 v[140:141], v140 offset0:3 offset1:4
	v_mfma_f32_32x32x16_bf16 v[116:131], v[152:155], v[208:211], v[116:131]
	v_mfma_f32_32x32x16_bf16 v[52:67], v[184:187], v[196:199], v[52:67]
	v_mfma_f32_32x32x16_bf16 v[68:83], v[176:179], v[196:199], v[68:83]
	v_mfma_f32_32x32x16_bf16 v[84:99], v[168:171], v[196:199], v[84:99]
	v_mfma_f32_32x32x16_bf16 v[100:115], v[156:159], v[196:199], v[100:115]
	v_mfma_f32_32x32x16_bf16 v[2:17], v[148:151], v[196:199], v[2:17]
	s_sub_i32 s29, s14, 32
	s_cmp_lt_u32 s29, s16
	s_cselect_b32 s18, s29, s17
	s_ashr_i32 s19, s18, 31
	s_waitcnt lgkmcnt(0)
	v_alignbit_b32 v143, v141, v140, v35
	v_alignbit_b32 v142, v140, v135, v166
	v_alignbit_b32 v141, v135, v133, v1
	v_alignbit_b32 v140, v134, v132, v164
	v_lshl_add_u64 v[132:133], s[18:19], 1, v[232:233]
	global_load_dwordx4 v[208:211], v[132:133], off
	v_add_u32_e32 v132, 0xffffff80, v249
	v_mfma_f32_32x32x16_bf16 v[116:131], v[140:143], v[196:199], v[116:131]
	v_and_b32_e32 v132, -4, v132
	s_waitcnt vmcnt(2)
	v_mfma_f32_32x32x16_bf16 v[18:33], v[136:139], v[192:195], v[18:33]
	v_add_u32_e32 v136, s0, v132
	ds_read2_b32 v[132:133], v136 offset1:1
	ds_read2_b32 v[134:135], v136 offset0:1 offset1:2
	ds_read2_b32 v[136:137], v136 offset0:3 offset1:4
	v_mfma_f32_32x32x16_bf16 v[36:51], v[204:207], v[192:195], v[36:51]
	v_mfma_f32_32x32x16_bf16 v[52:67], v[188:191], v[192:195], v[52:67]
	v_mfma_f32_32x32x16_bf16 v[68:83], v[180:183], v[192:195], v[68:83]
	v_mfma_f32_32x32x16_bf16 v[84:99], v[172:175], v[192:195], v[84:99]
	v_mfma_f32_32x32x16_bf16 v[100:115], v[160:163], v[192:195], v[100:115]
	v_mfma_f32_32x32x16_bf16 v[2:17], v[152:155], v[192:195], v[2:17]
	s_add_i32 s17, s14, -16
	s_cmp_lt_u32 s17, s16
	s_cselect_b32 s18, s17, s20
	s_ashr_i32 s19, s18, 31
	s_waitcnt lgkmcnt(1)
	v_alignbit_b32 v145, v135, v133, v1
	v_alignbit_b32 v144, v134, v132, v164
	v_lshl_add_u64 v[132:133], s[18:19], 1, v[232:233]
	global_load_dwordx4 v[196:199], v[132:133], off
	s_waitcnt lgkmcnt(0)
	v_alignbit_b32 v147, v137, v136, v35
	v_alignbit_b32 v146, v136, v135, v166
	v_add_u32_e32 v132, 0xffffffa0, v249
	s_waitcnt vmcnt(2)
	v_mfma_f32_32x32x16_bf16 v[18:33], v[200:203], v[250:253], v[18:33]
	v_and_b32_e32 v132, -4, v132
	v_add_u32_e32 v134, s0, v132
	ds_read2_b32 v[132:133], v134 offset1:1
	ds_read2_b32 v[136:137], v134 offset0:1 offset1:2
	ds_read2_b32 v[134:135], v134 offset0:3 offset1:4
	v_mfma_f32_32x32x16_bf16 v[116:131], v[144:147], v[192:195], v[116:131]
	v_mfma_f32_32x32x16_bf16 v[36:51], v[184:187], v[250:253], v[36:51]
	v_mfma_f32_32x32x16_bf16 v[52:67], v[176:179], v[250:253], v[52:67]
	v_mfma_f32_32x32x16_bf16 v[68:83], v[168:171], v[250:253], v[68:83]
	v_mfma_f32_32x32x16_bf16 v[84:99], v[156:159], v[250:253], v[84:99]
	v_mfma_f32_32x32x16_bf16 v[100:115], v[148:151], v[250:253], v[100:115]
	v_mfma_f32_32x32x16_bf16 v[2:17], v[140:143], v[250:253], v[2:17]
	s_cmp_lt_u32 s14, s16
	s_cselect_b32 s18, s14, s29
	s_ashr_i32 s19, s18, 31
	s_waitcnt lgkmcnt(0)
	v_alignbit_b32 v135, v135, v134, v35
	v_alignbit_b32 v134, v134, v137, v166
	v_alignbit_b32 v133, v137, v133, v1
	v_alignbit_b32 v132, v136, v132, v164
	v_lshl_add_u64 v[136:137], s[18:19], 1, v[232:233]
	global_load_dwordx4 v[192:195], v[136:137], off
	v_subrev_u32_e32 v136, 64, v249
	v_mfma_f32_32x32x16_bf16 v[116:131], v[132:135], v[250:253], v[116:131]
	v_and_b32_e32 v136, -4, v136
	v_add_u32_e32 v138, s0, v136
	ds_read2_b32 v[136:137], v138 offset1:1
	ds_read2_b32 v[200:201], v138 offset0:1 offset1:2
	ds_read2_b32 v[138:139], v138 offset0:3 offset1:4
	s_waitcnt vmcnt(2)
	v_mfma_f32_32x32x16_bf16 v[18:33], v[204:207], v[208:211], v[18:33]
	v_mfma_f32_32x32x16_bf16 v[36:51], v[188:191], v[208:211], v[36:51]
	v_mfma_f32_32x32x16_bf16 v[52:67], v[180:183], v[208:211], v[52:67]
	v_mfma_f32_32x32x16_bf16 v[68:83], v[172:175], v[208:211], v[68:83]
	v_mfma_f32_32x32x16_bf16 v[84:99], v[160:163], v[208:211], v[84:99]
	v_mfma_f32_32x32x16_bf16 v[100:115], v[152:155], v[208:211], v[100:115]
	v_mfma_f32_32x32x16_bf16 v[2:17], v[144:147], v[208:211], v[2:17]
	s_waitcnt lgkmcnt(0)
	v_alignbit_b32 v139, v139, v138, v35
	v_alignbit_b32 v138, v138, v201, v166
	v_alignbit_b32 v137, v201, v137, v1
	v_alignbit_b32 v136, v200, v136, v164
	s_add_i32 s1, s1, -1
	s_addk_i32 s14, 0x100
	v_mfma_f32_32x32x16_bf16 v[116:131], v[136:139], v[208:211], v[116:131]
	s_cmp_lg_u32 s1, 0
	s_cbranch_scc1 .LBB0_817
	s_add_i32 s0, s15, s37
	s_ashr_i32 s1, s0, 31
	s_lshl_b64 s[0:1], s[0:1], 2
	s_add_u32 s0, s42, s0
	s_addc_u32 s1, s43, s1
	global_load_dword v132, v34, s[0:1]
	s_mov_b64 s[0:1], -1
	s_and_b64 vcc, exec, s[2:3]
	s_cbranch_vccz .LBB0_820
	v_mad_i64_i32 v[134:135], s[0:1], s15, v243, v[214:215]
	v_lshlrev_b64 v[134:135], 1, v[134:135]
	v_lshl_add_u64 v[136:137], v[222:223], 0, v[134:135]
	v_lshl_add_u64 v[134:135], v[224:225], 0, v[134:135]
	s_mov_b64 s[0:1], 0
	global_load_dwordx2 v[154:155], v[136:137], off
	global_load_dwordx2 v[156:157], v[134:135], off
	global_load_dwordx2 v[158:159], v[136:137], off offset:16
	global_load_dwordx2 v[160:161], v[134:135], off offset:16
	global_load_dwordx2 v[162:163], v[136:137], off offset:32
	global_load_dwordx2 v[168:169], v[134:135], off offset:32
	global_load_dwordx2 v[170:171], v[136:137], off offset:48
	global_load_dwordx2 v[172:173], v[134:135], off offset:48
	global_load_dwordx2 v[174:175], v[136:137], off offset:64
	global_load_dwordx2 v[176:177], v[134:135], off offset:64
	global_load_dwordx2 v[178:179], v[136:137], off offset:80
	global_load_dwordx2 v[180:181], v[134:135], off offset:80
	global_load_dwordx2 v[182:183], v[136:137], off offset:96
	global_load_dwordx2 v[184:185], v[134:135], off offset:96
	global_load_dwordx2 v[186:187], v[136:137], off offset:112
	global_load_dwordx2 v[188:189], v[134:135], off offset:112
	global_load_dwordx2 v[200:201], v[136:137], off offset:128
	global_load_dwordx2 v[202:203], v[134:135], off offset:128
	global_load_dwordx2 v[206:207], v[136:137], off offset:144
	global_load_dwordx2 v[208:209], v[134:135], off offset:144
	global_load_dwordx2 v[210:211], v[136:137], off offset:160
	global_load_dwordx2 v[232:233], v[134:135], off offset:160
	global_load_dwordx2 v[248:249], v[136:137], off offset:176
	global_load_dwordx2 v[250:251], v[134:135], off offset:176
	s_waitcnt vmcnt(22)
	v_lshlrev_b32_e32 v144, 16, v154
	v_and_b32_e32 v145, 0xffff0000, v154
	v_lshlrev_b32_e32 v138, 16, v155
	v_and_b32_e32 v139, 0xffff0000, v155
	v_lshlrev_b32_e32 v142, 16, v156
	v_and_b32_e32 v143, 0xffff0000, v156
	v_pk_fma_f32 v[144:145], v[132:133], v[144:145], v[116:117] op_sel_hi:[0,1,1]
	v_lshlrev_b32_e32 v140, 16, v157
	v_and_b32_e32 v141, 0xffff0000, v157
	v_pk_fma_f32 v[138:139], v[132:133], v[138:139], v[118:119] op_sel_hi:[0,1,1]
	v_pk_mul_f32 v[142:143], v[144:145], v[142:143]
	v_pk_mul_f32 v[138:139], v[138:139], v[140:141]
	v_cvt_pk_bf16_f32 v140, v142, v143
	v_cvt_pk_bf16_f32 v141, v138, v139
	global_store_dwordx2 v[134:135], v[140:141], off
	s_waitcnt vmcnt(21)
	v_lshlrev_b32_e32 v144, 16, v158
	v_and_b32_e32 v145, 0xffff0000, v158
	v_lshlrev_b32_e32 v138, 16, v159
	v_and_b32_e32 v139, 0xffff0000, v159
	v_lshlrev_b32_e32 v142, 16, v160
	v_and_b32_e32 v143, 0xffff0000, v160
	v_pk_fma_f32 v[144:145], v[132:133], v[144:145], v[120:121] op_sel_hi:[0,1,1]
	v_lshlrev_b32_e32 v140, 16, v161
	v_and_b32_e32 v141, 0xffff0000, v161
	v_pk_fma_f32 v[138:139], v[132:133], v[138:139], v[122:123] op_sel_hi:[0,1,1]
	v_pk_mul_f32 v[142:143], v[144:145], v[142:143]
	v_pk_mul_f32 v[138:139], v[138:139], v[140:141]
	v_cvt_pk_bf16_f32 v140, v142, v143
	v_cvt_pk_bf16_f32 v141, v138, v139
	global_store_dwordx2 v[134:135], v[140:141], off offset:16
	s_waitcnt vmcnt(20)
	v_lshlrev_b32_e32 v144, 16, v162
	v_and_b32_e32 v145, 0xffff0000, v162
	v_lshlrev_b32_e32 v138, 16, v163
	v_and_b32_e32 v139, 0xffff0000, v163
	v_lshlrev_b32_e32 v142, 16, v168
	v_and_b32_e32 v143, 0xffff0000, v168
	v_pk_fma_f32 v[144:145], v[132:133], v[144:145], v[124:125] op_sel_hi:[0,1,1]
	v_lshlrev_b32_e32 v140, 16, v169
	v_and_b32_e32 v141, 0xffff0000, v169
	v_pk_fma_f32 v[138:139], v[132:133], v[138:139], v[126:127] op_sel_hi:[0,1,1]
	v_pk_mul_f32 v[142:143], v[144:145], v[142:143]
	v_pk_mul_f32 v[138:139], v[138:139], v[140:141]
	v_cvt_pk_bf16_f32 v140, v142, v143
	v_cvt_pk_bf16_f32 v141, v138, v139
	global_store_dwordx2 v[134:135], v[140:141], off offset:32
	s_waitcnt vmcnt(19)
	v_lshlrev_b32_e32 v144, 16, v170
	v_and_b32_e32 v145, 0xffff0000, v170
	v_lshlrev_b32_e32 v138, 16, v171
	v_and_b32_e32 v139, 0xffff0000, v171
	v_lshlrev_b32_e32 v142, 16, v172
	v_and_b32_e32 v143, 0xffff0000, v172
	v_pk_fma_f32 v[144:145], v[132:133], v[144:145], v[128:129] op_sel_hi:[0,1,1]
	v_lshlrev_b32_e32 v140, 16, v173
	v_and_b32_e32 v141, 0xffff0000, v173
	v_pk_fma_f32 v[138:139], v[132:133], v[138:139], v[130:131] op_sel_hi:[0,1,1]
	v_pk_mul_f32 v[142:143], v[144:145], v[142:143]
	v_pk_mul_f32 v[138:139], v[138:139], v[140:141]
	v_cvt_pk_bf16_f32 v140, v142, v143
	v_cvt_pk_bf16_f32 v141, v138, v139
	global_store_dwordx2 v[134:135], v[140:141], off offset:48
	s_waitcnt vmcnt(18)
	v_lshlrev_b32_e32 v144, 16, v174
	v_and_b32_e32 v145, 0xffff0000, v174
	v_lshlrev_b32_e32 v138, 16, v175
	v_and_b32_e32 v139, 0xffff0000, v175
	v_lshlrev_b32_e32 v142, 16, v176
	v_and_b32_e32 v143, 0xffff0000, v176
	v_pk_fma_f32 v[144:145], v[132:133], v[144:145], v[2:3] op_sel_hi:[0,1,1]
	v_lshlrev_b32_e32 v140, 16, v177
	v_and_b32_e32 v141, 0xffff0000, v177
	v_pk_fma_f32 v[138:139], v[132:133], v[138:139], v[4:5] op_sel_hi:[0,1,1]
	v_pk_mul_f32 v[142:143], v[144:145], v[142:143]
	v_pk_mul_f32 v[138:139], v[138:139], v[140:141]
	v_cvt_pk_bf16_f32 v140, v142, v143
	v_cvt_pk_bf16_f32 v141, v138, v139
	global_store_dwordx2 v[134:135], v[140:141], off offset:64
	s_waitcnt vmcnt(17)
	v_lshlrev_b32_e32 v144, 16, v178
	v_and_b32_e32 v145, 0xffff0000, v178
	v_lshlrev_b32_e32 v138, 16, v179
	v_and_b32_e32 v139, 0xffff0000, v179
	v_lshlrev_b32_e32 v142, 16, v180
	v_and_b32_e32 v143, 0xffff0000, v180
	v_pk_fma_f32 v[144:145], v[132:133], v[144:145], v[6:7] op_sel_hi:[0,1,1]
	v_lshlrev_b32_e32 v140, 16, v181
	v_and_b32_e32 v141, 0xffff0000, v181
	v_pk_fma_f32 v[138:139], v[132:133], v[138:139], v[8:9] op_sel_hi:[0,1,1]
	v_pk_mul_f32 v[142:143], v[144:145], v[142:143]
	v_pk_mul_f32 v[138:139], v[138:139], v[140:141]
	v_cvt_pk_bf16_f32 v140, v142, v143
	v_cvt_pk_bf16_f32 v141, v138, v139
	global_store_dwordx2 v[134:135], v[140:141], off offset:80
	s_waitcnt vmcnt(16)
	v_lshlrev_b32_e32 v144, 16, v182
	v_and_b32_e32 v145, 0xffff0000, v182
	v_lshlrev_b32_e32 v138, 16, v183
	v_and_b32_e32 v139, 0xffff0000, v183
	v_lshlrev_b32_e32 v142, 16, v184
	v_and_b32_e32 v143, 0xffff0000, v184
	v_pk_fma_f32 v[144:145], v[132:133], v[144:145], v[10:11] op_sel_hi:[0,1,1]
	v_lshlrev_b32_e32 v140, 16, v185
	v_and_b32_e32 v141, 0xffff0000, v185
	v_pk_fma_f32 v[138:139], v[132:133], v[138:139], v[12:13] op_sel_hi:[0,1,1]
	v_pk_mul_f32 v[142:143], v[144:145], v[142:143]
	v_pk_mul_f32 v[138:139], v[138:139], v[140:141]
	v_cvt_pk_bf16_f32 v140, v142, v143
	v_cvt_pk_bf16_f32 v141, v138, v139
	global_store_dwordx2 v[134:135], v[140:141], off offset:96
	s_waitcnt vmcnt(15)
	v_lshlrev_b32_e32 v144, 16, v186
	v_and_b32_e32 v145, 0xffff0000, v186
	v_lshlrev_b32_e32 v138, 16, v187
	v_and_b32_e32 v139, 0xffff0000, v187
	v_lshlrev_b32_e32 v142, 16, v188
	v_and_b32_e32 v143, 0xffff0000, v188
	v_pk_fma_f32 v[144:145], v[132:133], v[144:145], v[14:15] op_sel_hi:[0,1,1]
	v_lshlrev_b32_e32 v140, 16, v189
	v_and_b32_e32 v141, 0xffff0000, v189
	v_pk_fma_f32 v[138:139], v[132:133], v[138:139], v[16:17] op_sel_hi:[0,1,1]
	v_pk_mul_f32 v[142:143], v[144:145], v[142:143]
	v_pk_mul_f32 v[138:139], v[138:139], v[140:141]
	v_cvt_pk_bf16_f32 v140, v142, v143
	v_cvt_pk_bf16_f32 v141, v138, v139
	global_store_dwordx2 v[134:135], v[140:141], off offset:112
	s_waitcnt vmcnt(14)
	v_lshlrev_b32_e32 v144, 16, v200
	v_and_b32_e32 v145, 0xffff0000, v200
	v_lshlrev_b32_e32 v138, 16, v201
	v_and_b32_e32 v139, 0xffff0000, v201
	v_lshlrev_b32_e32 v142, 16, v202
	v_and_b32_e32 v143, 0xffff0000, v202
	v_pk_fma_f32 v[144:145], v[132:133], v[144:145], v[100:101] op_sel_hi:[0,1,1]
	v_lshlrev_b32_e32 v140, 16, v203
	v_and_b32_e32 v141, 0xffff0000, v203
	v_pk_fma_f32 v[138:139], v[132:133], v[138:139], v[102:103] op_sel_hi:[0,1,1]
	v_pk_mul_f32 v[142:143], v[144:145], v[142:143]
	v_pk_mul_f32 v[138:139], v[138:139], v[140:141]
	v_cvt_pk_bf16_f32 v140, v142, v143
	v_cvt_pk_bf16_f32 v141, v138, v139
	global_store_dwordx2 v[134:135], v[140:141], off offset:128
	s_waitcnt vmcnt(13)
	v_lshlrev_b32_e32 v144, 16, v206
	v_and_b32_e32 v145, 0xffff0000, v206
	v_lshlrev_b32_e32 v138, 16, v207
	v_and_b32_e32 v139, 0xffff0000, v207
	v_lshlrev_b32_e32 v142, 16, v208
	v_and_b32_e32 v143, 0xffff0000, v208
	v_pk_fma_f32 v[144:145], v[132:133], v[144:145], v[104:105] op_sel_hi:[0,1,1]
	v_lshlrev_b32_e32 v140, 16, v209
	v_and_b32_e32 v141, 0xffff0000, v209
	v_pk_fma_f32 v[138:139], v[132:133], v[138:139], v[106:107] op_sel_hi:[0,1,1]
	v_pk_mul_f32 v[142:143], v[144:145], v[142:143]
	v_pk_mul_f32 v[138:139], v[138:139], v[140:141]
	v_cvt_pk_bf16_f32 v140, v142, v143
	v_cvt_pk_bf16_f32 v141, v138, v139
	global_store_dwordx2 v[134:135], v[140:141], off offset:144
	s_waitcnt vmcnt(12)
	v_lshlrev_b32_e32 v144, 16, v210
	v_and_b32_e32 v145, 0xffff0000, v210
	v_lshlrev_b32_e32 v138, 16, v211
	v_and_b32_e32 v139, 0xffff0000, v211
	v_lshlrev_b32_e32 v142, 16, v232
	v_and_b32_e32 v143, 0xffff0000, v232
	v_pk_fma_f32 v[144:145], v[132:133], v[144:145], v[108:109] op_sel_hi:[0,1,1]
	v_lshlrev_b32_e32 v140, 16, v233
	v_and_b32_e32 v141, 0xffff0000, v233
	v_pk_fma_f32 v[138:139], v[132:133], v[138:139], v[110:111] op_sel_hi:[0,1,1]
	v_pk_mul_f32 v[142:143], v[144:145], v[142:143]
	v_pk_mul_f32 v[138:139], v[138:139], v[140:141]
	v_cvt_pk_bf16_f32 v140, v142, v143
	v_cvt_pk_bf16_f32 v141, v138, v139
	global_store_dwordx2 v[134:135], v[140:141], off offset:160
	s_waitcnt vmcnt(11)
	v_lshlrev_b32_e32 v144, 16, v248
	v_and_b32_e32 v145, 0xffff0000, v248
	v_lshlrev_b32_e32 v138, 16, v249
	v_and_b32_e32 v139, 0xffff0000, v249
	v_lshlrev_b32_e32 v142, 16, v250
	v_and_b32_e32 v143, 0xffff0000, v250
	v_pk_fma_f32 v[144:145], v[132:133], v[144:145], v[112:113] op_sel_hi:[0,1,1]
	v_lshlrev_b32_e32 v140, 16, v251
	v_and_b32_e32 v141, 0xffff0000, v251
	v_pk_fma_f32 v[138:139], v[132:133], v[138:139], v[114:115] op_sel_hi:[0,1,1]
	v_pk_mul_f32 v[142:143], v[144:145], v[142:143]
	v_pk_mul_f32 v[138:139], v[138:139], v[140:141]
	v_cvt_pk_bf16_f32 v140, v142, v143
	v_cvt_pk_bf16_f32 v141, v138, v139
	global_store_dwordx2 v[134:135], v[140:141], off offset:176
	global_load_dwordx2 v[154:155], v[136:137], off offset:192
	global_load_dwordx2 v[156:157], v[134:135], off offset:192
	global_load_dwordx2 v[158:159], v[136:137], off offset:208
	global_load_dwordx2 v[160:161], v[134:135], off offset:208
	global_load_dwordx2 v[162:163], v[136:137], off offset:224
	global_load_dwordx2 v[168:169], v[134:135], off offset:224
	global_load_dwordx2 v[170:171], v[136:137], off offset:240
	global_load_dwordx2 v[172:173], v[134:135], off offset:240
	global_load_dwordx2 v[174:175], v[136:137], off offset:256
	global_load_dwordx2 v[176:177], v[134:135], off offset:256
	global_load_dwordx2 v[178:179], v[136:137], off offset:272
	global_load_dwordx2 v[180:181], v[134:135], off offset:272
	global_load_dwordx2 v[182:183], v[136:137], off offset:288
	global_load_dwordx2 v[184:185], v[134:135], off offset:288
	global_load_dwordx2 v[186:187], v[136:137], off offset:304
	global_load_dwordx2 v[188:189], v[134:135], off offset:304
	global_load_dwordx2 v[200:201], v[136:137], off offset:320
	global_load_dwordx2 v[202:203], v[134:135], off offset:320
	global_load_dwordx2 v[206:207], v[136:137], off offset:336
	global_load_dwordx2 v[208:209], v[134:135], off offset:336
	global_load_dwordx2 v[210:211], v[136:137], off offset:352
	global_load_dwordx2 v[232:233], v[134:135], off offset:352
	global_load_dwordx2 v[248:249], v[136:137], off offset:368
	global_load_dwordx2 v[250:251], v[134:135], off offset:368
	s_waitcnt vmcnt(22)
	v_lshlrev_b32_e32 v144, 16, v154
	v_and_b32_e32 v145, 0xffff0000, v154
	v_lshlrev_b32_e32 v138, 16, v155
	v_and_b32_e32 v139, 0xffff0000, v155
	v_lshlrev_b32_e32 v142, 16, v156
	v_and_b32_e32 v143, 0xffff0000, v156
	v_pk_fma_f32 v[144:145], v[132:133], v[144:145], v[84:85] op_sel_hi:[0,1,1]
	v_lshlrev_b32_e32 v140, 16, v157
	v_and_b32_e32 v141, 0xffff0000, v157
	v_pk_fma_f32 v[138:139], v[132:133], v[138:139], v[86:87] op_sel_hi:[0,1,1]
	v_pk_mul_f32 v[142:143], v[144:145], v[142:143]
	v_pk_mul_f32 v[138:139], v[138:139], v[140:141]
	v_cvt_pk_bf16_f32 v140, v142, v143
	v_cvt_pk_bf16_f32 v141, v138, v139
	global_store_dwordx2 v[134:135], v[140:141], off offset:192
	s_waitcnt vmcnt(21)
	v_lshlrev_b32_e32 v144, 16, v158
	v_and_b32_e32 v145, 0xffff0000, v158
	v_lshlrev_b32_e32 v138, 16, v159
	v_and_b32_e32 v139, 0xffff0000, v159
	v_lshlrev_b32_e32 v142, 16, v160
	v_and_b32_e32 v143, 0xffff0000, v160
	v_pk_fma_f32 v[144:145], v[132:133], v[144:145], v[88:89] op_sel_hi:[0,1,1]
	v_lshlrev_b32_e32 v140, 16, v161
	v_and_b32_e32 v141, 0xffff0000, v161
	v_pk_fma_f32 v[138:139], v[132:133], v[138:139], v[90:91] op_sel_hi:[0,1,1]
	v_pk_mul_f32 v[142:143], v[144:145], v[142:143]
	v_pk_mul_f32 v[138:139], v[138:139], v[140:141]
	v_cvt_pk_bf16_f32 v140, v142, v143
	v_cvt_pk_bf16_f32 v141, v138, v139
	global_store_dwordx2 v[134:135], v[140:141], off offset:208
	s_waitcnt vmcnt(20)
	v_lshlrev_b32_e32 v144, 16, v162
	v_and_b32_e32 v145, 0xffff0000, v162
	v_lshlrev_b32_e32 v138, 16, v163
	v_and_b32_e32 v139, 0xffff0000, v163
	v_lshlrev_b32_e32 v142, 16, v168
	v_and_b32_e32 v143, 0xffff0000, v168
	v_pk_fma_f32 v[144:145], v[132:133], v[144:145], v[92:93] op_sel_hi:[0,1,1]
	v_lshlrev_b32_e32 v140, 16, v169
	v_and_b32_e32 v141, 0xffff0000, v169
	v_pk_fma_f32 v[138:139], v[132:133], v[138:139], v[94:95] op_sel_hi:[0,1,1]
	v_pk_mul_f32 v[142:143], v[144:145], v[142:143]
	v_pk_mul_f32 v[138:139], v[138:139], v[140:141]
	v_cvt_pk_bf16_f32 v140, v142, v143
	v_cvt_pk_bf16_f32 v141, v138, v139
	global_store_dwordx2 v[134:135], v[140:141], off offset:224
	s_waitcnt vmcnt(19)
	v_lshlrev_b32_e32 v144, 16, v170
	v_and_b32_e32 v145, 0xffff0000, v170
	v_lshlrev_b32_e32 v138, 16, v171
	v_and_b32_e32 v139, 0xffff0000, v171
	v_lshlrev_b32_e32 v142, 16, v172
	v_and_b32_e32 v143, 0xffff0000, v172
	v_pk_fma_f32 v[144:145], v[132:133], v[144:145], v[96:97] op_sel_hi:[0,1,1]
	v_lshlrev_b32_e32 v140, 16, v173
	v_and_b32_e32 v141, 0xffff0000, v173
	v_pk_fma_f32 v[138:139], v[132:133], v[138:139], v[98:99] op_sel_hi:[0,1,1]
	v_pk_mul_f32 v[142:143], v[144:145], v[142:143]
	v_pk_mul_f32 v[138:139], v[138:139], v[140:141]
	v_cvt_pk_bf16_f32 v140, v142, v143
	v_cvt_pk_bf16_f32 v141, v138, v139
	global_store_dwordx2 v[134:135], v[140:141], off offset:240
	s_waitcnt vmcnt(18)
	v_lshlrev_b32_e32 v144, 16, v174
	v_and_b32_e32 v145, 0xffff0000, v174
	v_lshlrev_b32_e32 v138, 16, v175
	v_and_b32_e32 v139, 0xffff0000, v175
	v_lshlrev_b32_e32 v142, 16, v176
	v_and_b32_e32 v143, 0xffff0000, v176
	v_pk_fma_f32 v[144:145], v[132:133], v[144:145], v[68:69] op_sel_hi:[0,1,1]
	v_lshlrev_b32_e32 v140, 16, v177
	v_and_b32_e32 v141, 0xffff0000, v177
	v_pk_fma_f32 v[138:139], v[132:133], v[138:139], v[70:71] op_sel_hi:[0,1,1]
	v_pk_mul_f32 v[142:143], v[144:145], v[142:143]
	v_pk_mul_f32 v[138:139], v[138:139], v[140:141]
	v_cvt_pk_bf16_f32 v140, v142, v143
	v_cvt_pk_bf16_f32 v141, v138, v139
	global_store_dwordx2 v[134:135], v[140:141], off offset:256
	s_waitcnt vmcnt(17)
	v_lshlrev_b32_e32 v144, 16, v178
	v_and_b32_e32 v145, 0xffff0000, v178
	v_lshlrev_b32_e32 v138, 16, v179
	v_and_b32_e32 v139, 0xffff0000, v179
	v_lshlrev_b32_e32 v142, 16, v180
	v_and_b32_e32 v143, 0xffff0000, v180
	v_pk_fma_f32 v[144:145], v[132:133], v[144:145], v[72:73] op_sel_hi:[0,1,1]
	v_lshlrev_b32_e32 v140, 16, v181
	v_and_b32_e32 v141, 0xffff0000, v181
	v_pk_fma_f32 v[138:139], v[132:133], v[138:139], v[74:75] op_sel_hi:[0,1,1]
	v_pk_mul_f32 v[142:143], v[144:145], v[142:143]
	v_pk_mul_f32 v[138:139], v[138:139], v[140:141]
	v_cvt_pk_bf16_f32 v140, v142, v143
	v_cvt_pk_bf16_f32 v141, v138, v139
	global_store_dwordx2 v[134:135], v[140:141], off offset:272
	s_waitcnt vmcnt(16)
	v_lshlrev_b32_e32 v144, 16, v182
	v_and_b32_e32 v145, 0xffff0000, v182
	v_lshlrev_b32_e32 v138, 16, v183
	v_and_b32_e32 v139, 0xffff0000, v183
	v_lshlrev_b32_e32 v142, 16, v184
	v_and_b32_e32 v143, 0xffff0000, v184
	v_pk_fma_f32 v[144:145], v[132:133], v[144:145], v[76:77] op_sel_hi:[0,1,1]
	v_lshlrev_b32_e32 v140, 16, v185
	v_and_b32_e32 v141, 0xffff0000, v185
	v_pk_fma_f32 v[138:139], v[132:133], v[138:139], v[78:79] op_sel_hi:[0,1,1]
	v_pk_mul_f32 v[142:143], v[144:145], v[142:143]
	v_pk_mul_f32 v[138:139], v[138:139], v[140:141]
	v_cvt_pk_bf16_f32 v140, v142, v143
	v_cvt_pk_bf16_f32 v141, v138, v139
	global_store_dwordx2 v[134:135], v[140:141], off offset:288
	s_waitcnt vmcnt(15)
	v_lshlrev_b32_e32 v144, 16, v186
	v_and_b32_e32 v145, 0xffff0000, v186
	v_lshlrev_b32_e32 v138, 16, v187
	v_and_b32_e32 v139, 0xffff0000, v187
	v_lshlrev_b32_e32 v142, 16, v188
	v_and_b32_e32 v143, 0xffff0000, v188
	v_pk_fma_f32 v[144:145], v[132:133], v[144:145], v[80:81] op_sel_hi:[0,1,1]
	v_lshlrev_b32_e32 v140, 16, v189
	v_and_b32_e32 v141, 0xffff0000, v189
	v_pk_fma_f32 v[138:139], v[132:133], v[138:139], v[82:83] op_sel_hi:[0,1,1]
	v_pk_mul_f32 v[142:143], v[144:145], v[142:143]
	v_pk_mul_f32 v[138:139], v[138:139], v[140:141]
	v_cvt_pk_bf16_f32 v140, v142, v143
	v_cvt_pk_bf16_f32 v141, v138, v139
	global_store_dwordx2 v[134:135], v[140:141], off offset:304
	s_waitcnt vmcnt(14)
	v_lshlrev_b32_e32 v144, 16, v200
	v_and_b32_e32 v145, 0xffff0000, v200
	v_lshlrev_b32_e32 v138, 16, v201
	v_and_b32_e32 v139, 0xffff0000, v201
	v_lshlrev_b32_e32 v142, 16, v202
	v_and_b32_e32 v143, 0xffff0000, v202
	v_pk_fma_f32 v[144:145], v[132:133], v[144:145], v[52:53] op_sel_hi:[0,1,1]
	v_lshlrev_b32_e32 v140, 16, v203
	v_and_b32_e32 v141, 0xffff0000, v203
	v_pk_fma_f32 v[138:139], v[132:133], v[138:139], v[54:55] op_sel_hi:[0,1,1]
	v_pk_mul_f32 v[142:143], v[144:145], v[142:143]
	v_pk_mul_f32 v[138:139], v[138:139], v[140:141]
	v_cvt_pk_bf16_f32 v140, v142, v143
	v_cvt_pk_bf16_f32 v141, v138, v139
	global_store_dwordx2 v[134:135], v[140:141], off offset:320
	s_waitcnt vmcnt(13)
	v_lshlrev_b32_e32 v144, 16, v206
	v_and_b32_e32 v145, 0xffff0000, v206
	v_lshlrev_b32_e32 v138, 16, v207
	v_and_b32_e32 v139, 0xffff0000, v207
	v_lshlrev_b32_e32 v142, 16, v208
	v_and_b32_e32 v143, 0xffff0000, v208
	v_pk_fma_f32 v[144:145], v[132:133], v[144:145], v[56:57] op_sel_hi:[0,1,1]
	v_lshlrev_b32_e32 v140, 16, v209
	v_and_b32_e32 v141, 0xffff0000, v209
	v_pk_fma_f32 v[138:139], v[132:133], v[138:139], v[58:59] op_sel_hi:[0,1,1]
	v_pk_mul_f32 v[142:143], v[144:145], v[142:143]
	v_pk_mul_f32 v[138:139], v[138:139], v[140:141]
	v_cvt_pk_bf16_f32 v140, v142, v143
	v_cvt_pk_bf16_f32 v141, v138, v139
	global_store_dwordx2 v[134:135], v[140:141], off offset:336
	s_waitcnt vmcnt(12)
	v_lshlrev_b32_e32 v144, 16, v210
	v_and_b32_e32 v145, 0xffff0000, v210
	v_lshlrev_b32_e32 v138, 16, v211
	v_and_b32_e32 v139, 0xffff0000, v211
	v_lshlrev_b32_e32 v142, 16, v232
	v_and_b32_e32 v143, 0xffff0000, v232
	v_pk_fma_f32 v[144:145], v[132:133], v[144:145], v[60:61] op_sel_hi:[0,1,1]
	v_lshlrev_b32_e32 v140, 16, v233
	v_and_b32_e32 v141, 0xffff0000, v233
	v_pk_fma_f32 v[138:139], v[132:133], v[138:139], v[62:63] op_sel_hi:[0,1,1]
	v_pk_mul_f32 v[142:143], v[144:145], v[142:143]
	v_pk_mul_f32 v[138:139], v[138:139], v[140:141]
	v_cvt_pk_bf16_f32 v140, v142, v143
	v_cvt_pk_bf16_f32 v141, v138, v139
	global_store_dwordx2 v[134:135], v[140:141], off offset:352
	s_waitcnt vmcnt(11)
	v_lshlrev_b32_e32 v144, 16, v248
	v_and_b32_e32 v145, 0xffff0000, v248
	v_lshlrev_b32_e32 v138, 16, v249
	v_and_b32_e32 v139, 0xffff0000, v249
	v_lshlrev_b32_e32 v142, 16, v250
	v_and_b32_e32 v143, 0xffff0000, v250
	v_pk_fma_f32 v[144:145], v[132:133], v[144:145], v[64:65] op_sel_hi:[0,1,1]
	v_lshlrev_b32_e32 v140, 16, v251
	v_and_b32_e32 v141, 0xffff0000, v251
	v_pk_fma_f32 v[138:139], v[132:133], v[138:139], v[66:67] op_sel_hi:[0,1,1]
	v_pk_mul_f32 v[142:143], v[144:145], v[142:143]
	v_pk_mul_f32 v[138:139], v[138:139], v[140:141]
	v_cvt_pk_bf16_f32 v140, v142, v143
	v_cvt_pk_bf16_f32 v141, v138, v139
	global_store_dwordx2 v[134:135], v[140:141], off offset:368
	global_load_dwordx2 v[154:155], v[136:137], off offset:384
	global_load_dwordx2 v[156:157], v[134:135], off offset:384
	global_load_dwordx2 v[158:159], v[136:137], off offset:400
	global_load_dwordx2 v[160:161], v[134:135], off offset:400
	global_load_dwordx2 v[162:163], v[136:137], off offset:416
	global_load_dwordx2 v[168:169], v[134:135], off offset:416
	global_load_dwordx2 v[170:171], v[136:137], off offset:432
	global_load_dwordx2 v[172:173], v[134:135], off offset:432
	global_load_dwordx2 v[174:175], v[136:137], off offset:448
	global_load_dwordx2 v[176:177], v[134:135], off offset:448
	global_load_dwordx2 v[178:179], v[136:137], off offset:464
	global_load_dwordx2 v[180:181], v[134:135], off offset:464
	global_load_dwordx2 v[182:183], v[136:137], off offset:480
	global_load_dwordx2 v[184:185], v[134:135], off offset:480
	global_load_dwordx2 v[186:187], v[136:137], off offset:496
	global_load_dwordx2 v[188:189], v[134:135], off offset:496
	s_waitcnt vmcnt(14)
	v_lshlrev_b32_e32 v144, 16, v154
	v_and_b32_e32 v145, 0xffff0000, v154
	v_lshlrev_b32_e32 v138, 16, v155
	v_and_b32_e32 v139, 0xffff0000, v155
	v_lshlrev_b32_e32 v142, 16, v156
	v_and_b32_e32 v143, 0xffff0000, v156
	v_pk_fma_f32 v[144:145], v[132:133], v[144:145], v[36:37] op_sel_hi:[0,1,1]
	v_lshlrev_b32_e32 v140, 16, v157
	v_and_b32_e32 v141, 0xffff0000, v157
	v_pk_fma_f32 v[138:139], v[132:133], v[138:139], v[38:39] op_sel_hi:[0,1,1]
	v_pk_mul_f32 v[142:143], v[144:145], v[142:143]
	v_pk_mul_f32 v[138:139], v[138:139], v[140:141]
	v_cvt_pk_bf16_f32 v140, v142, v143
	v_cvt_pk_bf16_f32 v141, v138, v139
	global_store_dwordx2 v[134:135], v[140:141], off offset:384
	s_waitcnt vmcnt(13)
	v_lshlrev_b32_e32 v144, 16, v158
	v_and_b32_e32 v145, 0xffff0000, v158
	v_lshlrev_b32_e32 v138, 16, v159
	v_and_b32_e32 v139, 0xffff0000, v159
	v_lshlrev_b32_e32 v142, 16, v160
	v_and_b32_e32 v143, 0xffff0000, v160
	v_pk_fma_f32 v[144:145], v[132:133], v[144:145], v[40:41] op_sel_hi:[0,1,1]
	v_lshlrev_b32_e32 v140, 16, v161
	v_and_b32_e32 v141, 0xffff0000, v161
	v_pk_fma_f32 v[138:139], v[132:133], v[138:139], v[42:43] op_sel_hi:[0,1,1]
	v_pk_mul_f32 v[142:143], v[144:145], v[142:143]
	v_pk_mul_f32 v[138:139], v[138:139], v[140:141]
	v_cvt_pk_bf16_f32 v140, v142, v143
	v_cvt_pk_bf16_f32 v141, v138, v139
	global_store_dwordx2 v[134:135], v[140:141], off offset:400
	s_waitcnt vmcnt(12)
	v_lshlrev_b32_e32 v144, 16, v162
	v_and_b32_e32 v145, 0xffff0000, v162
	v_lshlrev_b32_e32 v138, 16, v163
	v_and_b32_e32 v139, 0xffff0000, v163
	v_lshlrev_b32_e32 v142, 16, v168
	v_and_b32_e32 v143, 0xffff0000, v168
	v_pk_fma_f32 v[144:145], v[132:133], v[144:145], v[44:45] op_sel_hi:[0,1,1]
	v_lshlrev_b32_e32 v140, 16, v169
	v_and_b32_e32 v141, 0xffff0000, v169
	v_pk_fma_f32 v[138:139], v[132:133], v[138:139], v[46:47] op_sel_hi:[0,1,1]
	v_pk_mul_f32 v[142:143], v[144:145], v[142:143]
	v_pk_mul_f32 v[138:139], v[138:139], v[140:141]
	v_cvt_pk_bf16_f32 v140, v142, v143
	v_cvt_pk_bf16_f32 v141, v138, v139
	global_store_dwordx2 v[134:135], v[140:141], off offset:416
	s_waitcnt vmcnt(11)
	v_lshlrev_b32_e32 v144, 16, v170
	v_and_b32_e32 v145, 0xffff0000, v170
	v_lshlrev_b32_e32 v138, 16, v171
	v_and_b32_e32 v139, 0xffff0000, v171
	v_lshlrev_b32_e32 v142, 16, v172
	v_and_b32_e32 v143, 0xffff0000, v172
	v_pk_fma_f32 v[144:145], v[132:133], v[144:145], v[48:49] op_sel_hi:[0,1,1]
	v_lshlrev_b32_e32 v140, 16, v173
	v_and_b32_e32 v141, 0xffff0000, v173
	v_pk_fma_f32 v[138:139], v[132:133], v[138:139], v[50:51] op_sel_hi:[0,1,1]
	v_pk_mul_f32 v[142:143], v[144:145], v[142:143]
	v_pk_mul_f32 v[138:139], v[138:139], v[140:141]
	v_cvt_pk_bf16_f32 v140, v142, v143
	v_cvt_pk_bf16_f32 v141, v138, v139
	global_store_dwordx2 v[134:135], v[140:141], off offset:432
	s_waitcnt vmcnt(10)
	v_lshlrev_b32_e32 v144, 16, v174
	v_and_b32_e32 v145, 0xffff0000, v174
	v_lshlrev_b32_e32 v138, 16, v175
	v_and_b32_e32 v139, 0xffff0000, v175
	v_lshlrev_b32_e32 v142, 16, v176
	v_and_b32_e32 v143, 0xffff0000, v176
	v_pk_fma_f32 v[144:145], v[132:133], v[144:145], v[18:19] op_sel_hi:[0,1,1]
	v_lshlrev_b32_e32 v140, 16, v177
	v_and_b32_e32 v141, 0xffff0000, v177
	v_pk_fma_f32 v[138:139], v[132:133], v[138:139], v[20:21] op_sel_hi:[0,1,1]
	v_pk_mul_f32 v[142:143], v[144:145], v[142:143]
	v_pk_mul_f32 v[138:139], v[138:139], v[140:141]
	v_cvt_pk_bf16_f32 v140, v142, v143
	v_cvt_pk_bf16_f32 v141, v138, v139
	global_store_dwordx2 v[134:135], v[140:141], off offset:448
	s_waitcnt vmcnt(9)
	v_lshlrev_b32_e32 v144, 16, v178
	v_and_b32_e32 v145, 0xffff0000, v178
	v_lshlrev_b32_e32 v138, 16, v179
	v_and_b32_e32 v139, 0xffff0000, v179
	v_lshlrev_b32_e32 v142, 16, v180
	v_and_b32_e32 v143, 0xffff0000, v180
	v_pk_fma_f32 v[144:145], v[132:133], v[144:145], v[22:23] op_sel_hi:[0,1,1]
	v_lshlrev_b32_e32 v140, 16, v181
	v_and_b32_e32 v141, 0xffff0000, v181
	v_pk_fma_f32 v[138:139], v[132:133], v[138:139], v[24:25] op_sel_hi:[0,1,1]
	v_pk_mul_f32 v[142:143], v[144:145], v[142:143]
	v_pk_mul_f32 v[138:139], v[138:139], v[140:141]
	v_cvt_pk_bf16_f32 v140, v142, v143
	v_cvt_pk_bf16_f32 v141, v138, v139
	global_store_dwordx2 v[134:135], v[140:141], off offset:464
	s_waitcnt vmcnt(8)
	v_lshlrev_b32_e32 v144, 16, v182
	v_and_b32_e32 v145, 0xffff0000, v182
	v_lshlrev_b32_e32 v138, 16, v183
	v_and_b32_e32 v139, 0xffff0000, v183
	v_lshlrev_b32_e32 v142, 16, v184
	v_and_b32_e32 v143, 0xffff0000, v184
	v_pk_fma_f32 v[144:145], v[132:133], v[144:145], v[26:27] op_sel_hi:[0,1,1]
	v_lshlrev_b32_e32 v140, 16, v185
	v_and_b32_e32 v141, 0xffff0000, v185
	v_pk_fma_f32 v[138:139], v[132:133], v[138:139], v[28:29] op_sel_hi:[0,1,1]
	v_pk_mul_f32 v[142:143], v[144:145], v[142:143]
	v_pk_mul_f32 v[138:139], v[138:139], v[140:141]
	v_cvt_pk_bf16_f32 v140, v142, v143
	v_cvt_pk_bf16_f32 v141, v138, v139
	global_store_dwordx2 v[134:135], v[140:141], off offset:480
	s_waitcnt vmcnt(7)
	v_lshlrev_b32_e32 v144, 16, v186
	v_and_b32_e32 v145, 0xffff0000, v186
	v_lshlrev_b32_e32 v138, 16, v187
	v_and_b32_e32 v139, 0xffff0000, v187
	v_lshlrev_b32_e32 v142, 16, v188
	v_and_b32_e32 v143, 0xffff0000, v188
	v_pk_fma_f32 v[144:145], v[132:133], v[144:145], v[30:31] op_sel_hi:[0,1,1]
	v_lshlrev_b32_e32 v140, 16, v189
	v_and_b32_e32 v141, 0xffff0000, v189
	v_pk_fma_f32 v[138:139], v[132:133], v[138:139], v[32:33] op_sel_hi:[0,1,1]
	v_pk_mul_f32 v[142:143], v[144:145], v[142:143]
	v_pk_mul_f32 v[138:139], v[138:139], v[140:141]
	v_cvt_pk_bf16_f32 v140, v142, v143
	v_cvt_pk_bf16_f32 v141, v138, v139
	global_store_dwordx2 v[134:135], v[140:141], off offset:496
